# two-block item takes block A's C operand from four equal registers instead of sixteen fills
# speedup vs baseline: 1.0040x; 1.0005x over previous
; template <bool SELMASK>
; __device__ __forceinline__ void attn_far_fast(const LAS unsigned char* kb, const LAS unsigned char* vb, const bf16x8 (&qf)[2][2], int col, int q, float bias_far, bool sel0, bool sel1, Softmax (&st)[2], f32x4 (&O)[2][4]) {
;     ...
;     for (int kt = 0; kt < 4; ++kt) { const bf16x8 k0 = lds_frag(kb, 16 * kt + col, q), k1 = lds_frag(kb, 16 * kt + col, 4 + q);
; #pragma unroll
;         for (int c = 0; c < 2; ++c) { S[c][kt] = __builtin_amdgcn_mfma_f32_16x16x32_bf16(k0, qf[c][0], z4, 0, 0, 0); S[c][kt] = __builtin_amdgcn_mfma_f32_16x16x32_bf16(k1, qf[c][1], S[c][kt], 0, 0, 0); } }
;     bf16x8 pf[2][2];
; #pragma unroll
;     for (int c = 0; c < 2; ++c) {
;         const bool sel = c == 0 ? sel0 : sel1;
;         const float off = ((SELMASK && !sel) ? NEG : bias_far) - st[c].m;
.Lbm_full_f:
	v_add_u32_e32 v148, s83, v192
	v_add_u32_e32 v149, v148, v195
	v_add_u32_e32 v148, v148, v193
	ds_read_b128 v[116:119], v148
	ds_read_b128 v[120:123], v149
	ds_read_b128 v[124:127], v148 offset:2048
	ds_read_b128 v[128:131], v149 offset:2048
	ds_read_b128 v[132:135], v148 offset:4096
	ds_read_b128 v[136:139], v149 offset:4096
	ds_read_b128 v[140:143], v148 offset:6144
	ds_read_b128 v[144:147], v149 offset:6144
	s_add_i32 s32, s1, 0x2000
	s_and_b32 s32, s32, 0x6000
	v_add_u32_e32 v208, s32, v192
	v_add_u32_e32 v209, v208, v195
	v_add_u32_e32 v208, v208, v193
	ds_read_b128 v[38:41], v208
	ds_read_b128 v[42:45], v209
	ds_read_b128 v[46:49], v208 offset:2048
	ds_read_b128 v[50:53], v209 offset:2048
	s_waitcnt lgkmcnt(12)
	v_sub_f32_e32 v81, v81, v199
	v_sub_f32_e32 v82, v82, v199
	v_mov_b32_e32 v100, v81
	v_mov_b32_e32 v101, v81
	v_mov_b32_e32 v102, v81
	v_mov_b32_e32 v103, v81
	s_mov_b32 s83, -1
	s_add_i32 s77, s75, 2
	s_cmp_gt_i32 s77, s26
	s_cbranch_scc1 .Lbm_g1_end_af
	s_lshr_b32 s21, s77, 5
	v_mov_b32_e32 v255, v242
	s_cmp_eq_u32 s21, 1
	s_cselect_b64 vcc, -1, 0
	v_cndmask_b32_e32 v255, v255, v243, vcc
	s_cmp_eq_u32 s21, 2
	s_cselect_b64 vcc, -1, 0
	v_cndmask_b32_e32 v255, v255, v244, vcc
	s_cmp_eq_u32 s21, 3
	s_cselect_b64 vcc, -1, 0
	v_cndmask_b32_e32 v255, v255, v245, vcc
	s_and_b32 s21, s77, 31
	s_lshl_b32 s21, 1, s21
	s_lshl_b32 s32, s21, 1
	v_and_b32_e32 v80, s21, v255
	v_cmp_ne_u32_e64 s[12:13], 0, v80
	v_and_b32_e32 v80, s32, v255
	v_cmp_ne_u32_e64 s[14:15], 0, v80
	s_nop 3
	s_or_b64 s[22:23], s[12:13], s[14:15]
	s_bcnt1_i32_b64 s11, s[22:23]
	s_add_i32 s11, s11, 3
	s_lshr_b32 s11, s11, 2
	s_cmp_ge_u32 s91, s11
	s_cbranch_scc1 .Lbm_g1_end_af
	s_add_i32 s83, s91, 8
	s_cmp_lt_u32 s83, s11
	s_cselect_b32 s83, 0x10000, 0
	s_add_i32 s83, s83, s75
	s_add_i32 s83, s83, 2
	s_andn2_b64 s[84:85], s[12:13], s[14:15]
	s_bcnt1_i32_b64 s77, s[84:85]
	v_mbcnt_lo_u32_b32 v80, s84, 0
	v_mbcnt_hi_u32_b32 v80, s85, v80
	v_mov_b32_e32 v255, s77
	s_and_b64 s[84:85], s[12:13], s[14:15]
	s_bcnt1_i32_b64 s32, s[84:85]
	v_mbcnt_lo_u32_b32 v255, s84, v255
	v_mbcnt_hi_u32_b32 v255, s85, v255
	s_add_i32 s77, s77, s32
	v_cndmask_b32_e64 v80, v80, v255, s[84:85]
	v_mov_b32_e32 v255, s77
	s_andn2_b64 s[84:85], s[14:15], s[12:13]
	v_mbcnt_lo_u32_b32 v255, s84, v255
	v_mbcnt_hi_u32_b32 v255, s85, v255
	s_nop 0
	v_cndmask_b32_e64 v80, v80, v255, s[84:85]
	v_cndmask_b32_e64 v78, 0, 1, s[12:13]
	v_cndmask_b32_e64 v255, 0, 2, s[14:15]
	v_or_b32_e32 v78, v78, v255
	v_and_b32_e32 v255, 63, v185
	v_lshl_or_b32 v78, v78, 6, v255
	s_lshl_b32 s77, s91, 6
	s_add_i32 s77, s77, 0x20900
	v_add_u32_e32 v255, s77, v80
	s_and_saveexec_b64 s[84:85], s[22:23]
	ds_write_b8 v255, v78
	s_mov_b64 exec, s[84:85]
	s_lshl_b32 s32, s91, 2
	s_bcnt1_i32_b64 s84, s[22:23]
	v_lshrrev_b32_e32 v78, 2, v250
	v_add_u32_e32 v78, s32, v78
	v_cmp_gt_u32_e32 vcc, s84, v78
	v_add_u32_e32 v255, s77, v78
	ds_read_u8 v251, v255
	v_cndmask_b32_e64 v254, -1, 0, vcc
; __device__ __forceinline__ float ex2(float x) { return __builtin_amdgcn_exp2f(x); }
; template <bool SELMASK>
; __device__ __forceinline__ void attn_far_fast(const LAS unsigned char* kb, const LAS unsigned char* vb, const bf16x8 (&qf)[2][2], int col, int q, float bias_far, bool sel0, bool sel1, Softmax (&st)[2], f32x4 (&O)[2][4]) {
;     ...
;     for (int kt = 0; kt < 4; ++kt) { const bf16x8 k0 = lds_frag(kb, 16 * kt + col, q), k1 = lds_frag(kb, 16 * kt + col, 4 + q);
; #pragma unroll
;         for (int c = 0; c < 2; ++c) { S[c][kt] = __builtin_amdgcn_mfma_f32_16x16x32_bf16(k0, qf[c][0], z4, 0, 0, 0); S[c][kt] = __builtin_amdgcn_mfma_f32_16x16x32_bf16(k1, qf[c][1], S[c][kt], 0, 0, 0); } }
;     bf16x8 pf[2][2];
; #pragma unroll
;     for (int c = 0; c < 2; ++c) {
;         const bool sel = c == 0 ? sel0 : sel1;
;         const float off = ((SELMASK && !sel) ? NEG : bias_far) - st[c].m;
; #pragma unroll
;         for (int kt = 0; kt < 4; ++kt) { f32x4 p = S[c][kt] + off;
; #pragma unroll
;             for (int e = 0; e < 4; ++e) p[e] = ex2(p[e]);
;             S[c][kt] = p; }
;         pf[c][0] = pack8(S[c][0], S[c][1]); pf[c][1] = pack8(S[c][2], S[c][3]);
;         st[c].l = __builtin_amdgcn_mfma_f32_16x16x32_bf16(ONES8, pf[c][0], st[c].l, 0, 0, 0); st[c].l = __builtin_amdgcn_mfma_f32_16x16x32_bf16(ONES8, pf[c][1], st[c].l, 0, 0, 0);
;     }
; #pragma unroll
;     for (int c32 = 0; c32 < 2; ++c32)
; #pragma unroll
;         for (int dt = 0; dt < 4; ++dt) { const bf16x8 vf = lds_frag(vb, 16 * dt + col, 4 * c32 + q);
;             O[0][dt] = __builtin_amdgcn_mfma_f32_16x16x32_bf16(vf, pf[0][c32], O[0][dt], 0, 0, 0);
;             O[1][dt] = __builtin_amdgcn_mfma_f32_16x16x32_bf16(vf, pf[1][c32], O[1][dt], 0, 0, 0); }
.Lbm_g1_end_af:
	s_waitcnt lgkmcnt(10)
	v_mfma_f32_16x16x32_bf16 v[70:73], v[116:119], v[104:107], v[100:103]
	v_mov_b32_e32 v54, v82
	v_mov_b32_e32 v55, v82
	v_mfma_f32_16x16x32_bf16 v[70:73], v[120:123], v[108:111], v[70:73]
	v_mov_b32_e32 v56, v82
	v_mov_b32_e32 v57, v82
	s_waitcnt lgkmcnt(8)
	v_mfma_f32_16x16x32_bf16 v[74:77], v[124:127], v[104:107], v[100:103]
	v_mov_b32_e32 v58, v82
	v_mov_b32_e32 v59, v82
	v_mfma_f32_16x16x32_bf16 v[74:77], v[128:131], v[108:111], v[74:77]
	v_mov_b32_e32 v60, v82
	v_mov_b32_e32 v61, v82
	ds_read_b128 v[116:119], v148 offset:32768
	ds_read_b128 v[120:123], v149 offset:32768
	ds_read_b128 v[124:127], v148 offset:34816
	ds_read_b128 v[128:131], v149 offset:34816
	s_waitcnt lgkmcnt(10)
	v_mfma_f32_16x16x32_bf16 v[200:203], v[132:135], v[104:107], v[100:103]
	v_mov_b32_e32 v62, v82
	v_mov_b32_e32 v63, v82
	v_mfma_f32_16x16x32_bf16 v[200:203], v[136:139], v[108:111], v[200:203]
	v_mov_b32_e32 v64, v82
	v_mov_b32_e32 v65, v82
	s_waitcnt lgkmcnt(8)
	v_mfma_f32_16x16x32_bf16 v[204:207], v[140:143], v[104:107], v[100:103]
	v_mov_b32_e32 v66, v82
	v_mov_b32_e32 v67, v82
	v_mfma_f32_16x16x32_bf16 v[204:207], v[144:147], v[108:111], v[204:207]
	v_mov_b32_e32 v68, v82
	v_mov_b32_e32 v69, v82
	ds_read_b128 v[132:135], v148 offset:36864
	ds_read_b128 v[136:139], v149 offset:36864
	ds_read_b128 v[140:143], v148 offset:38912
	ds_read_b128 v[144:147], v149 offset:38912
	s_waitcnt lgkmcnt(10)
	v_mfma_f32_16x16x32_bf16 v[54:57], v[38:41], v[104:107], v[54:57]
	v_exp_f32_e32 v70, v70
	v_exp_f32_e32 v71, v71
	v_mfma_f32_16x16x32_bf16 v[54:57], v[42:45], v[108:111], v[54:57]
	v_exp_f32_e32 v72, v72
	v_exp_f32_e32 v73, v73
	s_waitcnt lgkmcnt(8)
	v_mfma_f32_16x16x32_bf16 v[58:61], v[46:49], v[104:107], v[58:61]
	v_exp_f32_e32 v74, v74
	v_exp_f32_e32 v75, v75
	v_mfma_f32_16x16x32_bf16 v[58:61], v[50:53], v[108:111], v[58:61]
	v_exp_f32_e32 v76, v76
	v_exp_f32_e32 v77, v77
	ds_read_b128 v[38:41], v208 offset:4096
	ds_read_b128 v[42:45], v209 offset:4096
	ds_read_b128 v[46:49], v208 offset:6144
	ds_read_b128 v[50:53], v209 offset:6144
	v_cvt_pk_bf16_f32 v70, v70, v71
	v_cvt_pk_bf16_f32 v71, v72, v73
	v_cvt_pk_bf16_f32 v72, v74, v75
	v_cvt_pk_bf16_f32 v73, v76, v77
	s_nop 1
	s_waitcnt lgkmcnt(4)
	v_mfma_f32_16x16x32_bf16 v[100:103], v[112:115], v[70:73], 0
	v_exp_f32_e32 v200, v200
	v_exp_f32_e32 v201, v201
	v_mfma_f32_16x16x32_bf16 v[84:87], v[116:119], v[70:73], 0
	v_exp_f32_e32 v202, v202
	v_exp_f32_e32 v203, v203
	v_mfma_f32_16x16x32_bf16 v[88:91], v[124:127], v[70:73], 0
	v_exp_f32_e32 v204, v204
	v_exp_f32_e32 v205, v205
	v_mfma_f32_16x16x32_bf16 v[92:95], v[132:135], v[70:73], 0
	v_exp_f32_e32 v206, v206
	v_exp_f32_e32 v207, v207
	v_mfma_f32_16x16x32_bf16 v[96:99], v[140:143], v[70:73], 0
	v_cvt_pk_bf16_f32 v74, v200, v201
	v_cvt_pk_bf16_f32 v75, v202, v203
	v_cvt_pk_bf16_f32 v76, v204, v205
	v_cvt_pk_bf16_f32 v77, v206, v207
	s_waitcnt lgkmcnt(2)
	v_mfma_f32_16x16x32_bf16 v[62:65], v[38:41], v[104:107], v[62:65]
	v_exp_f32_e32 v54, v54
	v_exp_f32_e32 v55, v55
	v_mfma_f32_16x16x32_bf16 v[62:65], v[42:45], v[108:111], v[62:65]
	v_exp_f32_e32 v56, v56
	v_exp_f32_e32 v57, v57
	s_waitcnt lgkmcnt(0)
	v_mfma_f32_16x16x32_bf16 v[66:69], v[46:49], v[104:107], v[66:69]
	v_exp_f32_e32 v58, v58
	v_exp_f32_e32 v59, v59
	v_mfma_f32_16x16x32_bf16 v[66:69], v[50:53], v[108:111], v[66:69]
	v_exp_f32_e32 v60, v60
	v_exp_f32_e32 v61, v61
	v_mfma_f32_16x16x32_bf16 v[100:103], v[112:115], v[74:77], v[100:103]
	v_cvt_pk_bf16_f32 v54, v54, v55
	v_mfma_f32_16x16x32_bf16 v[84:87], v[120:123], v[74:77], v[84:87]
	v_cvt_pk_bf16_f32 v55, v56, v57
	v_mfma_f32_16x16x32_bf16 v[88:91], v[128:131], v[74:77], v[88:91]
	v_cvt_pk_bf16_f32 v56, v58, v59
	v_mfma_f32_16x16x32_bf16 v[92:95], v[136:139], v[74:77], v[92:95]
	v_cvt_pk_bf16_f32 v57, v60, v61
	v_mfma_f32_16x16x32_bf16 v[96:99], v[144:147], v[74:77], v[96:99]
	ds_read_b128 v[116:119], v208 offset:32768
	ds_read_b128 v[120:123], v209 offset:32768
	ds_read_b128 v[124:127], v208 offset:34816
	ds_read_b128 v[128:131], v209 offset:34816
	ds_read_b128 v[132:135], v208 offset:36864
	ds_read_b128 v[136:139], v209 offset:36864
	ds_read_b128 v[140:143], v208 offset:38912
	ds_read_b128 v[144:147], v209 offset:38912
	s_mov_b32 s100, -1
	s_cmp_lt_i32 s83, 0
	s_cbranch_scc1 .Lbm_g2_end_af
	s_waitcnt lgkmcnt(8)
	v_or_b32_e32 v251, v251, v254
	v_max_i32_e32 v254, 0, v251
	v_and_b32_e32 v254, 63, v254
	v_lshlrev_b32_e32 v254, 11, v254
	v_mov_b32_e32 v255, 0
	v_lshl_add_u64 v[254:255], v[254:255], 0, v[246:247]
	global_load_dwordx4 v[104:107], v[254:255], off
	global_load_dwordx4 v[108:111], v[254:255], off offset:64
	s_mov_b32 s100, s83

; __device__ __forceinline__ float ex2(float x) { return __builtin_amdgcn_exp2f(x); }
; template <bool SELMASK>
; __device__ __forceinline__ void attn_far_fast(const LAS unsigned char* kb, const LAS unsigned char* vb, const bf16x8 (&qf)[2][2], int col, int q, float bias_far, bool sel0, bool sel1, Softmax (&st)[2], f32x4 (&O)[2][4]) {
;     ...
;     for (int kt = 0; kt < 4; ++kt) { const bf16x8 k0 = lds_frag(kb, 16 * kt + col, q), k1 = lds_frag(kb, 16 * kt + col, 4 + q);
; #pragma unroll
;         for (int c = 0; c < 2; ++c) { S[c][kt] = __builtin_amdgcn_mfma_f32_16x16x32_bf16(k0, qf[c][0], z4, 0, 0, 0); S[c][kt] = __builtin_amdgcn_mfma_f32_16x16x32_bf16(k1, qf[c][1], S[c][kt], 0, 0, 0); } }
;     bf16x8 pf[2][2];
; #pragma unroll
;     for (int c = 0; c < 2; ++c) {
;         const bool sel = c == 0 ? sel0 : sel1;
;         const float off = ((SELMASK && !sel) ? NEG : bias_far) - st[c].m;
; #pragma unroll
;         for (int kt = 0; kt < 4; ++kt) { f32x4 p = S[c][kt] + off;
; #pragma unroll
;             for (int e = 0; e < 4; ++e) p[e] = ex2(p[e]);
;             S[c][kt] = p; }
;         pf[c][0] = pack8(S[c][0], S[c][1]); pf[c][1] = pack8(S[c][2], S[c][3]);
;         st[c].l = __builtin_amdgcn_mfma_f32_16x16x32_bf16(ONES8, pf[c][0], st[c].l, 0, 0, 0); st[c].l = __builtin_amdgcn_mfma_f32_16x16x32_bf16(ONES8, pf[c][1], st[c].l, 0, 0, 0);
;     }
; #pragma unroll
;     for (int c32 = 0; c32 < 2; ++c32)
; #pragma unroll
;         for (int dt = 0; dt < 4; ++dt) { const bf16x8 vf = lds_frag(vb, 16 * dt + col, 4 * c32 + q);
;             O[0][dt] = __builtin_amdgcn_mfma_f32_16x16x32_bf16(vf, pf[0][c32], O[0][dt], 0, 0, 0);
;             O[1][dt] = __builtin_amdgcn_mfma_f32_16x16x32_bf16(vf, pf[1][c32], O[1][dt], 0, 0, 0); }
.Lbm_r1_two:
	v_add_u32_e32 v148, s83, v192
	v_add_u32_e32 v149, v148, v195
	v_add_u32_e32 v148, v148, v193
	ds_read_b128 v[116:119], v148
	ds_read_b128 v[120:123], v149
	ds_read_b128 v[124:127], v148 offset:2048
	ds_read_b128 v[128:131], v149 offset:2048
	ds_read_b128 v[132:135], v148 offset:4096
	ds_read_b128 v[136:139], v149 offset:4096
	ds_read_b128 v[140:143], v148 offset:6144
	ds_read_b128 v[144:147], v149 offset:6144
	s_add_i32 s32, s1, 0x2000
	s_and_b32 s32, s32, 0x6000
	v_add_u32_e32 v208, s32, v192
	v_add_u32_e32 v209, v208, v195
	v_add_u32_e32 v208, v208, v193
	ds_read_b128 v[38:41], v208
	ds_read_b128 v[42:45], v209
	ds_read_b128 v[46:49], v208 offset:2048
	ds_read_b128 v[50:53], v209 offset:2048
	s_waitcnt lgkmcnt(12)
	v_sub_f32_e32 v81, v81, v199
	v_sub_f32_e32 v82, v82, v199
	v_mov_b32_e32 v100, v81
	v_mov_b32_e32 v101, v81
	v_mov_b32_e32 v102, v81
	v_mov_b32_e32 v103, v81
	s_waitcnt lgkmcnt(10)
	v_mfma_f32_16x16x32_bf16 v[70:73], v[116:119], v[104:107], v[100:103]
	v_mov_b32_e32 v54, v82
	v_mov_b32_e32 v55, v82
	v_mfma_f32_16x16x32_bf16 v[70:73], v[120:123], v[108:111], v[70:73]
	v_mov_b32_e32 v56, v82
	v_mov_b32_e32 v57, v82
	s_waitcnt lgkmcnt(8)
	v_mfma_f32_16x16x32_bf16 v[74:77], v[124:127], v[104:107], v[100:103]
	v_mov_b32_e32 v58, v82
	v_mov_b32_e32 v59, v82
	v_mfma_f32_16x16x32_bf16 v[74:77], v[128:131], v[108:111], v[74:77]
	v_mov_b32_e32 v60, v82
	v_mov_b32_e32 v61, v82
	ds_read_b128 v[116:119], v148 offset:32768
	ds_read_b128 v[120:123], v149 offset:32768
	ds_read_b128 v[124:127], v148 offset:34816
	ds_read_b128 v[128:131], v149 offset:34816
	s_waitcnt lgkmcnt(10)
	v_mfma_f32_16x16x32_bf16 v[200:203], v[132:135], v[104:107], v[100:103]
	v_mov_b32_e32 v62, v82
	v_mov_b32_e32 v63, v82
	v_mfma_f32_16x16x32_bf16 v[200:203], v[136:139], v[108:111], v[200:203]
	v_mov_b32_e32 v64, v82
	v_mov_b32_e32 v65, v82
	s_waitcnt lgkmcnt(8)
	v_mfma_f32_16x16x32_bf16 v[204:207], v[140:143], v[104:107], v[100:103]
	v_mov_b32_e32 v66, v82
	v_mov_b32_e32 v67, v82
	v_mfma_f32_16x16x32_bf16 v[204:207], v[144:147], v[108:111], v[204:207]
	v_mov_b32_e32 v68, v82
	v_mov_b32_e32 v69, v82
	ds_read_b128 v[132:135], v148 offset:36864
	ds_read_b128 v[136:139], v149 offset:36864
	ds_read_b128 v[140:143], v148 offset:38912
	ds_read_b128 v[144:147], v149 offset:38912
	s_waitcnt lgkmcnt(10)
	v_mfma_f32_16x16x32_bf16 v[54:57], v[38:41], v[104:107], v[54:57]
	v_exp_f32_e32 v70, v70
	v_exp_f32_e32 v71, v71
	v_mfma_f32_16x16x32_bf16 v[54:57], v[42:45], v[108:111], v[54:57]
	v_exp_f32_e32 v72, v72
	v_exp_f32_e32 v73, v73
	s_waitcnt lgkmcnt(8)
	v_mfma_f32_16x16x32_bf16 v[58:61], v[46:49], v[104:107], v[58:61]
	v_exp_f32_e32 v74, v74
	v_exp_f32_e32 v75, v75
	v_mfma_f32_16x16x32_bf16 v[58:61], v[50:53], v[108:111], v[58:61]
	v_exp_f32_e32 v76, v76
	v_exp_f32_e32 v77, v77
	ds_read_b128 v[38:41], v208 offset:4096
	ds_read_b128 v[42:45], v209 offset:4096
	ds_read_b128 v[46:49], v208 offset:6144
	ds_read_b128 v[50:53], v209 offset:6144
	v_cvt_pk_bf16_f32 v70, v70, v71
	v_cvt_pk_bf16_f32 v71, v72, v73
	v_cvt_pk_bf16_f32 v72, v74, v75
	v_cvt_pk_bf16_f32 v73, v76, v77
	s_nop 1
	s_waitcnt lgkmcnt(4)
	v_mfma_f32_16x16x32_bf16 v[100:103], v[112:115], v[70:73], 0
	v_exp_f32_e32 v200, v200
	v_exp_f32_e32 v201, v201
	v_mfma_f32_16x16x32_bf16 v[84:87], v[116:119], v[70:73], 0
	v_exp_f32_e32 v202, v202
	v_exp_f32_e32 v203, v203
	v_mfma_f32_16x16x32_bf16 v[88:91], v[124:127], v[70:73], 0
	v_exp_f32_e32 v204, v204
	v_exp_f32_e32 v205, v205
	v_mfma_f32_16x16x32_bf16 v[92:95], v[132:135], v[70:73], 0
	v_exp_f32_e32 v206, v206
	v_exp_f32_e32 v207, v207
	v_mfma_f32_16x16x32_bf16 v[96:99], v[140:143], v[70:73], 0
	v_cvt_pk_bf16_f32 v74, v200, v201
	v_cvt_pk_bf16_f32 v75, v202, v203
	v_cvt_pk_bf16_f32 v76, v204, v205
	v_cvt_pk_bf16_f32 v77, v206, v207
	s_waitcnt lgkmcnt(2)
	v_mfma_f32_16x16x32_bf16 v[62:65], v[38:41], v[104:107], v[62:65]
	v_exp_f32_e32 v54, v54
	v_exp_f32_e32 v55, v55
	v_mfma_f32_16x16x32_bf16 v[62:65], v[42:45], v[108:111], v[62:65]
	v_exp_f32_e32 v56, v56
	v_exp_f32_e32 v57, v57
	s_waitcnt lgkmcnt(0)
	v_mfma_f32_16x16x32_bf16 v[66:69], v[46:49], v[104:107], v[66:69]
	v_exp_f32_e32 v58, v58
	v_exp_f32_e32 v59, v59
	v_mfma_f32_16x16x32_bf16 v[66:69], v[50:53], v[108:111], v[66:69]
	v_exp_f32_e32 v60, v60
	v_exp_f32_e32 v61, v61
	v_mfma_f32_16x16x32_bf16 v[100:103], v[112:115], v[74:77], v[100:103]
	v_cvt_pk_bf16_f32 v54, v54, v55
	v_mfma_f32_16x16x32_bf16 v[84:87], v[120:123], v[74:77], v[84:87]
	v_cvt_pk_bf16_f32 v55, v56, v57
	v_mfma_f32_16x16x32_bf16 v[88:91], v[128:131], v[74:77], v[88:91]
	v_cvt_pk_bf16_f32 v56, v58, v59
	v_mfma_f32_16x16x32_bf16 v[92:95], v[136:139], v[74:77], v[92:95]
	v_cvt_pk_bf16_f32 v57, v60, v61
	v_mfma_f32_16x16x32_bf16 v[96:99], v[144:147], v[74:77], v[96:99]
	ds_read_b128 v[116:119], v208 offset:32768
	ds_read_b128 v[120:123], v209 offset:32768
	ds_read_b128 v[124:127], v208 offset:34816
	ds_read_b128 v[128:131], v209 offset:34816
	ds_read_b128 v[132:135], v208 offset:36864
	ds_read_b128 v[136:139], v209 offset:36864
	ds_read_b128 v[140:143], v208 offset:38912
	ds_read_b128 v[144:147], v209 offset:38912
	s_nop 3
	s_waitcnt lgkmcnt(0)
; __device__ __forceinline__ float ex2(float x) { return __builtin_amdgcn_exp2f(x); }
; template <bool SELMASK>
; __device__ __forceinline__ void attn_far_fast(const LAS unsigned char* kb, const LAS unsigned char* vb, const bf16x8 (&qf)[2][2], int col, int q, float bias_far, bool sel0, bool sel1, Softmax (&st)[2], f32x4 (&O)[2][4]) {
;     ...
;         for (int kt = 0; kt < 4; ++kt) { f32x4 p = S[c][kt] + off;
; #pragma unroll
;             for (int e = 0; e < 4; ++e) p[e] = ex2(p[e]);
;             S[c][kt] = p; }
;         pf[c][0] = pack8(S[c][0], S[c][1]); pf[c][1] = pack8(S[c][2], S[c][3]);
;         st[c].l = __builtin_amdgcn_mfma_f32_16x16x32_bf16(ONES8, pf[c][0], st[c].l, 0, 0, 0); st[c].l = __builtin_amdgcn_mfma_f32_16x16x32_bf16(ONES8, pf[c][1], st[c].l, 0, 0, 0);
;     }
; #pragma unroll
;     for (int c32 = 0; c32 < 2; ++c32)
; #pragma unroll
;         for (int dt = 0; dt < 4; ++dt) { const bf16x8 vf = lds_frag(vb, 16 * dt + col, 4 * c32 + q);
;             O[0][dt] = __builtin_amdgcn_mfma_f32_16x16x32_bf16(vf, pf[0][c32], O[0][dt], 0, 0, 0);
;             O[1][dt] = __builtin_amdgcn_mfma_f32_16x16x32_bf16(vf, pf[1][c32], O[1][dt], 0, 0, 0); }
	v_mfma_f32_16x16x32_bf16 v[100:103], v[112:115], v[54:57], v[100:103]
	v_exp_f32_e32 v62, v62
	v_exp_f32_e32 v63, v63
	v_mfma_f32_16x16x32_bf16 v[84:87], v[116:119], v[54:57], v[84:87]
	v_exp_f32_e32 v64, v64
	v_exp_f32_e32 v65, v65
	v_mfma_f32_16x16x32_bf16 v[88:91], v[124:127], v[54:57], v[88:91]
	v_exp_f32_e32 v66, v66
	v_exp_f32_e32 v67, v67
	v_mfma_f32_16x16x32_bf16 v[92:95], v[132:135], v[54:57], v[92:95]
	v_exp_f32_e32 v68, v68
	v_exp_f32_e32 v69, v69
	v_mfma_f32_16x16x32_bf16 v[96:99], v[140:143], v[54:57], v[96:99]
	v_cvt_pk_bf16_f32 v58, v62, v63
	v_cvt_pk_bf16_f32 v59, v64, v65
	v_cvt_pk_bf16_f32 v60, v66, v67
	v_cvt_pk_bf16_f32 v61, v68, v69
	v_lshlrev_b32_e32 v254, 6, v186
	v_sub_u32_e32 v254, v83, v254
	ds_read2_b32 v[200:201], v83 offset0:0 offset1:4
	ds_read2_b32 v[202:203], v83 offset0:8 offset1:12
	ds_read2_b32 v[204:205], v83 offset0:64 offset1:68
	ds_read2_b32 v[206:207], v83 offset0:72 offset1:76
	ds_read2_b32 v[62:63], v83 offset0:128 offset1:132
	ds_read2_b32 v[64:65], v83 offset0:136 offset1:140
	ds_read2_b32 v[66:67], v83 offset0:192 offset1:196
	ds_read2_b32 v[68:69], v83 offset0:200 offset1:204
	ds_read_b32 v199, v254 offset:1024
	v_mfma_f32_16x16x32_bf16 v[100:103], v[112:115], v[58:61], v[100:103]
	v_mfma_f32_16x16x32_bf16 v[84:87], v[120:123], v[58:61], v[84:87]
	v_mfma_f32_16x16x32_bf16 v[88:91], v[128:131], v[58:61], v[88:91]
	v_mfma_f32_16x16x32_bf16 v[92:95], v[136:139], v[58:61], v[92:95]
	v_mfma_f32_16x16x32_bf16 v[96:99], v[144:147], v[58:61], v[96:99]
	s_nop 1
	s_waitcnt lgkmcnt(0)
	v_add_f32_e32 v200, v200, v84
	v_add_f32_e32 v201, v201, v85
	v_add_f32_e32 v202, v202, v86
	v_add_f32_e32 v203, v203, v87
	v_add_f32_e32 v204, v204, v88
	v_add_f32_e32 v205, v205, v89
	v_add_f32_e32 v206, v206, v90
	v_add_f32_e32 v207, v207, v91
	v_add_f32_e32 v199, v199, v100
	v_add_f32_e32 v62, v62, v92
	v_add_f32_e32 v63, v63, v93
	v_add_f32_e32 v64, v64, v94
	v_add_f32_e32 v65, v65, v95
	v_add_f32_e32 v66, v66, v96
	v_add_f32_e32 v67, v67, v97
	v_add_f32_e32 v68, v68, v98
	v_add_f32_e32 v69, v69, v99
	v_cmp_ne_u32_e32 vcc, 0, v79
	s_and_saveexec_b64 s[84:85], vcc
	ds_write2_b32 v83, v200, v201 offset0:0 offset1:4
	ds_write2_b32 v83, v202, v203 offset0:8 offset1:12
	ds_write2_b32 v83, v204, v205 offset0:64 offset1:68
	ds_write2_b32 v83, v206, v207 offset0:72 offset1:76
	ds_write2_b32 v83, v62, v63 offset0:128 offset1:132
	ds_write2_b32 v83, v64, v65 offset0:136 offset1:140
	ds_write2_b32 v83, v66, v67 offset0:192 offset1:196
	ds_write2_b32 v83, v68, v69 offset0:200 offset1:204
	ds_write_b32 v254, v199 offset:1024
	s_mov_b64 exec, s[84:85]
	s_nop 3
	s_mov_b32 s100, -1
	s_add_i32 s21, s91, 8
	s_andn2_b64 s[84:85], s[12:13], s[14:15]
	s_bcnt1_i32_b64 s77, s[84:85]
	v_mbcnt_lo_u32_b32 v80, s84, 0
	v_mbcnt_hi_u32_b32 v80, s85, v80
	v_mov_b32_e32 v56, s77
	s_and_b64 s[84:85], s[12:13], s[14:15]
	s_bcnt1_i32_b64 s32, s[84:85]
	v_mbcnt_lo_u32_b32 v56, s84, v56
	v_mbcnt_hi_u32_b32 v56, s85, v56
	s_add_i32 s77, s77, s32
	v_cndmask_b32_e64 v80, v80, v56, s[84:85]
	v_mov_b32_e32 v56, s77
	s_andn2_b64 s[84:85], s[14:15], s[12:13]
	v_mbcnt_lo_u32_b32 v56, s84, v56
	v_mbcnt_hi_u32_b32 v56, s85, v56
	s_nop 0
	v_cndmask_b32_e64 v80, v80, v56, s[84:85]
	v_cndmask_b32_e64 v58, 0, 1, s[12:13]
	v_cndmask_b32_e64 v59, 0, 2, s[14:15]
	v_or_b32_e32 v58, v58, v59
	v_and_b32_e32 v59, 63, v185
	v_lshl_or_b32 v58, v58, 6, v59
	s_lshl_b32 s77, s91, 6
	s_add_i32 s77, s77, 0x20900
	v_add_u32_e32 v59, s77, v80
	s_and_saveexec_b64 s[84:85], s[22:23]
	ds_write_b8 v59, v58
	s_mov_b64 exec, s[84:85]
	s_lshl_b32 s32, s21, 2
	s_bcnt1_i32_b64 s84, s[22:23]
	v_lshrrev_b32_e32 v58, 2, v250
	v_add_u32_e32 v58, s32, v58
	v_cmp_gt_u32_e32 vcc, s84, v58
	v_add_u32_e32 v59, s77, v58
	ds_read_u8 v63, v59
	v_cndmask_b32_e64 v60, -1, 0, vcc
	s_waitcnt lgkmcnt(0)
	v_or_b32_e32 v63, v63, v60
	v_lshrrev_b32_e32 v56, 31, v63
	v_xor_b32_e32 v56, 1, v56
	v_max_i32_e32 v55, 0, v63
	v_mov_b32_e32 v79, v56
	v_and_b32_e32 v54, 63, v55
	v_bfe_u32 v58, v55, 6, 1
	v_bfe_u32 v59, v55, 7, 1
	v_lshlrev_b32_e32 v60, 11, v54
	v_mov_b32_e32 v61, 0
	v_lshl_add_u64 v[60:61], v[60:61], 0, v[246:247]
	global_load_dwordx4 v[104:107], v[60:61], off
	global_load_dwordx4 v[108:111], v[60:61], off offset:64
	v_lshl_add_u32 v63, v54, 4, v249
	ds_read_b32 v199, v63
	v_mul_u32_u24_e32 v83, 0x410, v54
	v_cmp_ne_u32_e32 vcc, 0, v58
	v_add_u32_e32 v83, v83, v248
	s_nop 0
	v_cndmask_b32_e32 v81, v2, v154, vcc
	s_cmp_lg_u64 vcc, 0
	s_cselect_b32 s21, 1, 0
	v_cmp_ne_u32_e32 vcc, 0, v59
	s_nop 1
	v_cndmask_b32_e32 v82, v2, v154, vcc
	s_cmp_lg_u64 vcc, 0
	s_cselect_b32 s32, 1, 0
	s_waitcnt vmcnt(0)
	s_and_b32 s83, s1, 0x4000
	v_add_u32_e32 v148, s83, v192
	v_add_u32_e32 v149, v148, v195
	v_add_u32_e32 v148, v148, v193
	ds_read_b128 v[116:119], v148
	ds_read_b128 v[120:123], v149
	ds_read_b128 v[124:127], v148 offset:2048
	ds_read_b128 v[128:131], v149 offset:2048
	ds_read_b128 v[132:135], v148 offset:4096
	ds_read_b128 v[136:139], v149 offset:4096
	ds_read_b128 v[140:143], v148 offset:6144
	ds_read_b128 v[144:147], v149 offset:6144
	s_add_i32 s32, s1, 0x2000
	s_and_b32 s32, s32, 0x6000
	v_add_u32_e32 v208, s32, v192
	v_add_u32_e32 v209, v208, v195
	v_add_u32_e32 v208, v208, v193
	ds_read_b128 v[38:41], v208
	ds_read_b128 v[42:45], v209
	ds_read_b128 v[46:49], v208 offset:2048
	ds_read_b128 v[50:53], v209 offset:2048
	s_waitcnt lgkmcnt(12)
	v_sub_f32_e32 v81, v81, v199
	v_sub_f32_e32 v82, v82, v199
	v_mov_b32_e32 v100, v81
	v_mov_b32_e32 v101, v81
	v_mov_b32_e32 v102, v81
	v_mov_b32_e32 v103, v81
	s_waitcnt lgkmcnt(10)
; __device__ __forceinline__ float ex2(float x) { return __builtin_amdgcn_exp2f(x); }
; template <bool SELMASK>
; __device__ __forceinline__ void attn_far_fast(const LAS unsigned char* kb, const LAS unsigned char* vb, const bf16x8 (&qf)[2][2], int col, int q, float bias_far, bool sel0, bool sel1, Softmax (&st)[2], f32x4 (&O)[2][4]) {
;     ...
;     for (int kt = 0; kt < 4; ++kt) { const bf16x8 k0 = lds_frag(kb, 16 * kt + col, q), k1 = lds_frag(kb, 16 * kt + col, 4 + q);
; #pragma unroll
;         for (int c = 0; c < 2; ++c) { S[c][kt] = __builtin_amdgcn_mfma_f32_16x16x32_bf16(k0, qf[c][0], z4, 0, 0, 0); S[c][kt] = __builtin_amdgcn_mfma_f32_16x16x32_bf16(k1, qf[c][1], S[c][kt], 0, 0, 0); } }
;     bf16x8 pf[2][2];
; #pragma unroll
;     for (int c = 0; c < 2; ++c) {
;         const bool sel = c == 0 ? sel0 : sel1;
;         const float off = ((SELMASK && !sel) ? NEG : bias_far) - st[c].m;
; #pragma unroll
;         for (int kt = 0; kt < 4; ++kt) { f32x4 p = S[c][kt] + off;
; #pragma unroll
;             for (int e = 0; e < 4; ++e) p[e] = ex2(p[e]);
;             S[c][kt] = p; }
;         pf[c][0] = pack8(S[c][0], S[c][1]); pf[c][1] = pack8(S[c][2], S[c][3]);
;         st[c].l = __builtin_amdgcn_mfma_f32_16x16x32_bf16(ONES8, pf[c][0], st[c].l, 0, 0, 0); st[c].l = __builtin_amdgcn_mfma_f32_16x16x32_bf16(ONES8, pf[c][1], st[c].l, 0, 0, 0);
;     }
; #pragma unroll
;     for (int c32 = 0; c32 < 2; ++c32)
; #pragma unroll
;         for (int dt = 0; dt < 4; ++dt) { const bf16x8 vf = lds_frag(vb, 16 * dt + col, 4 * c32 + q);
;             O[0][dt] = __builtin_amdgcn_mfma_f32_16x16x32_bf16(vf, pf[0][c32], O[0][dt], 0, 0, 0);
;             O[1][dt] = __builtin_amdgcn_mfma_f32_16x16x32_bf16(vf, pf[1][c32], O[1][dt], 0, 0, 0); }
	v_mfma_f32_16x16x32_bf16 v[70:73], v[116:119], v[104:107], v[100:103]
	v_mov_b32_e32 v54, v82
	v_mov_b32_e32 v55, v82
	v_mfma_f32_16x16x32_bf16 v[70:73], v[120:123], v[108:111], v[70:73]
	v_mov_b32_e32 v56, v82
	v_mov_b32_e32 v57, v82
	s_waitcnt lgkmcnt(8)
	v_mfma_f32_16x16x32_bf16 v[74:77], v[124:127], v[104:107], v[100:103]
	v_mov_b32_e32 v58, v82
	v_mov_b32_e32 v59, v82
	v_mfma_f32_16x16x32_bf16 v[74:77], v[128:131], v[108:111], v[74:77]
	v_mov_b32_e32 v60, v82
	v_mov_b32_e32 v61, v82
	ds_read_b128 v[116:119], v148 offset:32768
	ds_read_b128 v[120:123], v149 offset:32768
	ds_read_b128 v[124:127], v148 offset:34816
	ds_read_b128 v[128:131], v149 offset:34816
	s_waitcnt lgkmcnt(10)
	v_mfma_f32_16x16x32_bf16 v[200:203], v[132:135], v[104:107], v[100:103]
	v_mov_b32_e32 v62, v82
	v_mov_b32_e32 v63, v82
	v_mfma_f32_16x16x32_bf16 v[200:203], v[136:139], v[108:111], v[200:203]
	v_mov_b32_e32 v64, v82
	v_mov_b32_e32 v65, v82
	s_waitcnt lgkmcnt(8)
	v_mfma_f32_16x16x32_bf16 v[204:207], v[140:143], v[104:107], v[100:103]
	v_mov_b32_e32 v66, v82
	v_mov_b32_e32 v67, v82
	v_mfma_f32_16x16x32_bf16 v[204:207], v[144:147], v[108:111], v[204:207]
	v_mov_b32_e32 v68, v82
	v_mov_b32_e32 v69, v82
	ds_read_b128 v[132:135], v148 offset:36864
	ds_read_b128 v[136:139], v149 offset:36864
	ds_read_b128 v[140:143], v148 offset:38912
	ds_read_b128 v[144:147], v149 offset:38912
	s_waitcnt lgkmcnt(10)
	v_mfma_f32_16x16x32_bf16 v[54:57], v[38:41], v[104:107], v[54:57]
	v_exp_f32_e32 v70, v70
	v_exp_f32_e32 v71, v71
	v_mfma_f32_16x16x32_bf16 v[54:57], v[42:45], v[108:111], v[54:57]
	v_exp_f32_e32 v72, v72
	v_exp_f32_e32 v73, v73
	s_waitcnt lgkmcnt(8)
	v_mfma_f32_16x16x32_bf16 v[58:61], v[46:49], v[104:107], v[58:61]
	v_exp_f32_e32 v74, v74
	v_exp_f32_e32 v75, v75
	v_mfma_f32_16x16x32_bf16 v[58:61], v[50:53], v[108:111], v[58:61]
	v_exp_f32_e32 v76, v76
	v_exp_f32_e32 v77, v77
	ds_read_b128 v[38:41], v208 offset:4096
	ds_read_b128 v[42:45], v209 offset:4096
	ds_read_b128 v[46:49], v208 offset:6144
	ds_read_b128 v[50:53], v209 offset:6144
	v_cvt_pk_bf16_f32 v70, v70, v71
	v_cvt_pk_bf16_f32 v71, v72, v73
	v_cvt_pk_bf16_f32 v72, v74, v75
	v_cvt_pk_bf16_f32 v73, v76, v77
	s_nop 1
	s_waitcnt lgkmcnt(4)
	v_mfma_f32_16x16x32_bf16 v[100:103], v[112:115], v[70:73], 0
	v_exp_f32_e32 v200, v200
	v_exp_f32_e32 v201, v201
	v_mfma_f32_16x16x32_bf16 v[84:87], v[116:119], v[70:73], 0
	v_exp_f32_e32 v202, v202
	v_exp_f32_e32 v203, v203
	v_mfma_f32_16x16x32_bf16 v[88:91], v[124:127], v[70:73], 0
	v_exp_f32_e32 v204, v204
	v_exp_f32_e32 v205, v205
	v_mfma_f32_16x16x32_bf16 v[92:95], v[132:135], v[70:73], 0
	v_exp_f32_e32 v206, v206
	v_exp_f32_e32 v207, v207
	v_mfma_f32_16x16x32_bf16 v[96:99], v[140:143], v[70:73], 0
	v_cvt_pk_bf16_f32 v74, v200, v201
	v_cvt_pk_bf16_f32 v75, v202, v203
	v_cvt_pk_bf16_f32 v76, v204, v205
	v_cvt_pk_bf16_f32 v77, v206, v207
	s_waitcnt lgkmcnt(2)
	v_mfma_f32_16x16x32_bf16 v[62:65], v[38:41], v[104:107], v[62:65]
	v_exp_f32_e32 v54, v54
	v_exp_f32_e32 v55, v55
	v_mfma_f32_16x16x32_bf16 v[62:65], v[42:45], v[108:111], v[62:65]
	v_exp_f32_e32 v56, v56
	v_exp_f32_e32 v57, v57
	s_waitcnt lgkmcnt(0)
	v_mfma_f32_16x16x32_bf16 v[66:69], v[46:49], v[104:107], v[66:69]
	v_exp_f32_e32 v58, v58
	v_exp_f32_e32 v59, v59
	v_mfma_f32_16x16x32_bf16 v[66:69], v[50:53], v[108:111], v[66:69]
	v_exp_f32_e32 v60, v60
	v_exp_f32_e32 v61, v61
	v_mfma_f32_16x16x32_bf16 v[100:103], v[112:115], v[74:77], v[100:103]
	v_cvt_pk_bf16_f32 v54, v54, v55
	v_mfma_f32_16x16x32_bf16 v[84:87], v[120:123], v[74:77], v[84:87]
	v_cvt_pk_bf16_f32 v55, v56, v57
	v_mfma_f32_16x16x32_bf16 v[88:91], v[128:131], v[74:77], v[88:91]
	v_cvt_pk_bf16_f32 v56, v58, v59
	v_mfma_f32_16x16x32_bf16 v[92:95], v[136:139], v[74:77], v[92:95]
	v_cvt_pk_bf16_f32 v57, v60, v61
	v_mfma_f32_16x16x32_bf16 v[96:99], v[144:147], v[74:77], v[96:99]
	ds_read_b128 v[116:119], v208 offset:32768
	ds_read_b128 v[120:123], v209 offset:32768
	ds_read_b128 v[124:127], v208 offset:34816
	ds_read_b128 v[128:131], v209 offset:34816
	ds_read_b128 v[132:135], v208 offset:36864
	ds_read_b128 v[136:139], v209 offset:36864
	ds_read_b128 v[140:143], v208 offset:38912
	ds_read_b128 v[144:147], v209 offset:38912
	s_nop 3
	s_waitcnt lgkmcnt(0)
	v_mfma_f32_16x16x32_bf16 v[100:103], v[112:115], v[54:57], v[100:103]
	v_exp_f32_e32 v62, v62
	v_exp_f32_e32 v63, v63
	v_mfma_f32_16x16x32_bf16 v[84:87], v[116:119], v[54:57], v[84:87]
	v_exp_f32_e32 v64, v64
	v_exp_f32_e32 v65, v65
	v_mfma_f32_16x16x32_bf16 v[88:91], v[124:127], v[54:57], v[88:91]
	v_exp_f32_e32 v66, v66
	v_exp_f32_e32 v67, v67
	v_mfma_f32_16x16x32_bf16 v[92:95], v[132:135], v[54:57], v[92:95]
	v_exp_f32_e32 v68, v68
	v_exp_f32_e32 v69, v69
	v_mfma_f32_16x16x32_bf16 v[96:99], v[140:143], v[54:57], v[96:99]
	v_cvt_pk_bf16_f32 v58, v62, v63
	v_cvt_pk_bf16_f32 v59, v64, v65
	v_cvt_pk_bf16_f32 v60, v66, v67
	v_cvt_pk_bf16_f32 v61, v68, v69
	v_lshlrev_b32_e32 v254, 6, v186
	v_sub_u32_e32 v254, v83, v254
	ds_read2_b32 v[200:201], v83 offset0:0 offset1:4
	ds_read2_b32 v[202:203], v83 offset0:8 offset1:12
	ds_read2_b32 v[204:205], v83 offset0:64 offset1:68
	ds_read2_b32 v[206:207], v83 offset0:72 offset1:76
	ds_read2_b32 v[62:63], v83 offset0:128 offset1:132
	ds_read2_b32 v[64:65], v83 offset0:136 offset1:140
	ds_read2_b32 v[66:67], v83 offset0:192 offset1:196
	ds_read2_b32 v[68:69], v83 offset0:200 offset1:204
	ds_read_b32 v199, v254 offset:1024
	v_mfma_f32_16x16x32_bf16 v[100:103], v[112:115], v[58:61], v[100:103]
	v_mfma_f32_16x16x32_bf16 v[84:87], v[120:123], v[58:61], v[84:87]
	v_mfma_f32_16x16x32_bf16 v[88:91], v[128:131], v[58:61], v[88:91]
	v_mfma_f32_16x16x32_bf16 v[92:95], v[136:139], v[58:61], v[92:95]
	v_mfma_f32_16x16x32_bf16 v[96:99], v[144:147], v[58:61], v[96:99]
	s_nop 1
	s_waitcnt lgkmcnt(0)
	v_add_f32_e32 v200, v200, v84
	v_add_f32_e32 v201, v201, v85
	v_add_f32_e32 v202, v202, v86
	v_add_f32_e32 v203, v203, v87
	v_add_f32_e32 v204, v204, v88
	v_add_f32_e32 v205, v205, v89
	v_add_f32_e32 v206, v206, v90
	v_add_f32_e32 v207, v207, v91
	v_add_f32_e32 v199, v199, v100
	v_add_f32_e32 v62, v62, v92
	v_add_f32_e32 v63, v63, v93
	v_add_f32_e32 v64, v64, v94
	v_add_f32_e32 v65, v65, v95
	v_add_f32_e32 v66, v66, v96
	v_add_f32_e32 v67, v67, v97
	v_add_f32_e32 v68, v68, v98
	v_add_f32_e32 v69, v69, v99
	v_cmp_ne_u32_e32 vcc, 0, v79
	s_and_saveexec_b64 s[84:85], vcc
	ds_write2_b32 v83, v200, v201 offset0:0 offset1:4
	ds_write2_b32 v83, v202, v203 offset0:8 offset1:12
	ds_write2_b32 v83, v204, v205 offset0:64 offset1:68
	ds_write2_b32 v83, v206, v207 offset0:72 offset1:76
	ds_write2_b32 v83, v62, v63 offset0:128 offset1:132
	ds_write2_b32 v83, v64, v65 offset0:136 offset1:140
	ds_write2_b32 v83, v66, v67 offset0:192 offset1:196
	ds_write2_b32 v83, v68, v69 offset0:200 offset1:204
	ds_write_b32 v254, v199 offset:1024
	s_mov_b64 exec, s[84:85]
	s_nop 3
